# next-unit index prefetch made asynchronous in P3/P19/P13: the in-loop queue atomic returns straight into the qp.pre register; hipcc's vmcnt(0)+readfirstlane right after the atomic removed (the unit-ta
# speedup vs baseline: 1.0035x; 1.0035x over previous
; template <int MODE, int DQK, int DV>
; __device__ __forceinline__ void attn_pass(LAS unsigned char* lds, const Tens& T, size_t rowbase, int q0, f32x16 (&o)[DV / 32], float& l_out, const int wave, QPre* qp = nullptr) {
;     ...
;         if (qp != nullptr && it == (MODE == AM_FOX ? 1 : ntile - 4)) { if (tid == 0) qp->pre = __hip_atomic_fetch_add(qp->ctr, 1u, __ATOMIC_RELAXED, __HIP_MEMORY_SCOPE_AGENT); qp->issued = true; }
.LBB0_659:
	s_cmp_lg_u32 s72, 0
	s_cselect_b64 vcc, -1, 0
	v_cndmask_b32_e32 v103, 1, v103, vcc
	s_nor_b64 s[8:9], vcc, s[4:5]
	s_and_saveexec_b64 s[6:7], s[8:9]
	s_cbranch_execz .LBB0_663
	s_mov_b64 s[10:11], exec
	v_mbcnt_lo_u32_b32 v32, s10, 0
	v_mbcnt_hi_u32_b32 v32, s11, v32
	v_cmp_eq_u32_e32 vcc, 0, v32
	s_and_saveexec_b64 s[8:9], vcc
	s_cbranch_execz .LBB0_662
	s_bcnt1_i32_b64 s10, s[10:11]
	v_mov_b32_e32 v33, s10
	global_atomic_add v93, v83, v33, s[68:69] sc0
.LBB0_662:
	s_or_b64 exec, exec, s[8:9]
	v_mov_b32_e32 v103, 1

; template <int MODE, int DQK, int DV>
; __device__ __forceinline__ void attn_pass(LAS unsigned char* lds, const Tens& T, size_t rowbase, int q0, f32x16 (&o)[DV / 32], float& l_out, const int wave, QPre* qp = nullptr) {
;     ...
;         if (qp != nullptr && it == (MODE == AM_FOX ? 1 : ntile - 4)) { if (tid == 0) qp->pre = __hip_atomic_fetch_add(qp->ctr, 1u, __ATOMIC_RELAXED, __HIP_MEMORY_SCOPE_AGENT); qp->issued = true; }
.LBB0_1648:
	s_mov_b64 s[38:39], exec
	v_mbcnt_lo_u32_b32 v32, s38, 0
	v_mbcnt_hi_u32_b32 v32, s39, v32
	v_cmp_eq_u32_e32 vcc, 0, v32
	s_and_saveexec_b64 s[36:37], vcc
	s_cbranch_execz .LBB0_1650
	s_bcnt1_i32_b64 s0, s[38:39]
	v_mov_b32_e32 v33, s0
	global_atomic_add v94, v66, v33, s[16:17] sc0
.LBB0_1650:
	s_or_b64 exec, exec, s[36:37]
	v_mov_b32_e32 v103, 1
	s_or_b64 exec, exec, s[34:35]
	s_cmp_gt_u32 s10, s12
	s_cbranch_scc1 .LBB0_1625

; template <int MODE, int DQK, int DV>
; __device__ __forceinline__ void attn_pass(LAS unsigned char* lds, const Tens& T, size_t rowbase, int q0, f32x16 (&o)[DV / 32], float& l_out, const int wave, QPre* qp = nullptr) {
;     ...
;         if (qp != nullptr && it == (MODE == AM_FOX ? 1 : ntile - 4)) { if (tid == 0) qp->pre = __hip_atomic_fetch_add(qp->ctr, 1u, __ATOMIC_RELAXED, __HIP_MEMORY_SCOPE_AGENT); qp->issued = true; }
.LBB0_1665:
	s_or_b64 exec, exec, s[36:37]
	v_mov_b32_e32 v103, 1
	s_or_b64 exec, exec, s[34:35]
	s_add_i32 s0, s10, 2
	s_cmp_gt_u32 s0, s12
	s_cbranch_scc1 .LBB0_1634

; template <int MODE, int DQK, int DV>
; __device__ __forceinline__ void attn_pass(LAS unsigned char* lds, const Tens& T, size_t rowbase, int q0, f32x16 (&o)[DV / 32], float& l_out, const int wave, QPre* qp = nullptr) {
;     ...
;         if (qp != nullptr && it == (MODE == AM_FOX ? 1 : ntile - 4)) { if (tid == 0) qp->pre = __hip_atomic_fetch_add(qp->ctr, 1u, __ATOMIC_RELAXED, __HIP_MEMORY_SCOPE_AGENT); qp->issued = true; }
.LBB0_1675:
	s_mov_b64 s[36:37], exec
	v_mbcnt_lo_u32_b32 v32, s36, 0
	v_mbcnt_hi_u32_b32 v32, s37, v32
	v_cmp_eq_u32_e32 vcc, 0, v32
	s_and_saveexec_b64 s[34:35], vcc
	s_cbranch_execz .LBB0_1677
	s_bcnt1_i32_b64 s0, s[36:37]
	v_mov_b32_e32 v33, s0
	global_atomic_add v94, v66, v33, s[16:17] sc0
.LBB0_1677:
	s_or_b64 exec, exec, s[34:35]
	v_mov_b32_e32 v103, 1
	s_or_b64 exec, exec, s[30:31]
	s_add_i32 s0, s10, 4
	s_cmp_gt_u32 s0, s12
	s_cbranch_scc1 .LBB0_1643

; template <int MODE, int DQK, int DV>
; __device__ __forceinline__ void attn_pass(LAS unsigned char* lds, const Tens& T, size_t rowbase, int q0, f32x16 (&o)[DV / 32], float& l_out, const int wave, QPre* qp = nullptr) {
;     ...
;         if (qp != nullptr && it == (MODE == AM_FOX ? 1 : ntile - 4)) { if (tid == 0) qp->pre = __hip_atomic_fetch_add(qp->ctr, 1u, __ATOMIC_RELAXED, __HIP_MEMORY_SCOPE_AGENT); qp->issued = true; }
.LBB0_2545:
	s_mov_b64 s[10:11], exec
	v_mbcnt_lo_u32_b32 v0, s10, 0
	v_mbcnt_hi_u32_b32 v0, s11, v0
	v_cmp_eq_u32_e32 vcc, 0, v0
	s_and_saveexec_b64 s[8:9], vcc
	s_cbranch_execz .LBB0_2547
	s_bcnt1_i32_b64 s10, s[10:11]
	v_mov_b32_e32 v2, s10
	global_atomic_add v142, v1, v2, s[64:65] sc0
.LBB0_2547:
	s_or_b64 exec, exec, s[8:9]
	v_mov_b32_e32 v154, 1
	s_or_b64 exec, exec, s[6:7]
	s_cmp_gt_u32 s1, s74
	s_cbranch_scc1 .LBB0_2542

; template <int MODE, int DQK, int DV>
; __device__ __forceinline__ void attn_pass(LAS unsigned char* lds, const Tens& T, size_t rowbase, int q0, f32x16 (&o)[DV / 32], float& l_out, const int wave, QPre* qp = nullptr) {
;     ...
;         if (qp != nullptr && it == (MODE == AM_FOX ? 1 : ntile - 4)) { if (tid == 0) qp->pre = __hip_atomic_fetch_add(qp->ctr, 1u, __ATOMIC_RELAXED, __HIP_MEMORY_SCOPE_AGENT); qp->issued = true; }
.LBB0_2585:
	s_or_b64 exec, exec, s[8:9]
	v_mov_b32_e32 v154, 1
	s_or_b64 exec, exec, s[6:7]
	s_cmp_gt_u32 s46, s74
	s_cbranch_scc1 .LBB0_2580
